# compress GEMM: K split four ways over 64 workgroups (f32 partial slabs summed in the combine phase) instead of 16 workgroups
# speedup vs baseline: 1.0121x; 1.0121x over previous
;     __device__ __forceinline__ size_t a_off(const Unit& u, const Gemm& g) const { size_t o = (size_t)u.pm * BM * g.lda * 2; if (MODE == 1) o += (size_t)(u.pn >> 1) * 512 * 2; return o; }
;     __device__ __forceinline__ size_t b_off(const Unit& u, const Gemm& g) const { return (size_t)u.pn * BM * g.ldb * 2; }
; #define PG8_BAR __builtin_amdgcn_s_barrier()
; template <class Epi, class Sched, bool ALIGN_EPI = true, bool SP2 = true, class Side = NoSide>
; __device__ __forceinline__ void gemm_phase(LAS unsigned char* lds, const Gemm g, const Sched& S, const Epi& E, const Side side = Side()) {
;     ...
;     Unit cur, nxt; int ui = 0;
;     if (!S.next(0, cur)) return;
;     f32x4 acc[2][2][4][2];
; #pragma unroll
;     for (int a = 0; a < 2; ++a)
; #pragma unroll
;         for (int b = 0; b < 2; ++b)
; #pragma unroll
;             for (int m = 0; m < 4; ++m)
; #pragma unroll
;                 for (int n = 0; n < 2; ++n) acc[a][b][m][n] = (f32x4){0.f, 0.f, 0.f, 0.f};
;     bf16x8 At[4][2], B0[2][2], B1[2][2];
;     const char* cA = (const char*)g.A + S.a_off(cur, g); const char* cB = (const char*)g.Bt + S.b_off(cur, g);
;     if constexpr (SP2) {
;         PG8_STAGE(PG8_SB(0, 0), cB, voffB); PG8_STAGE(PG8_SB(0, 1), cB + hstepB, voffB); PG8_STAGE(PG8_SA(0, 0), cA, voffA); PG8_STAGE(PG8_SA(0, 1), cA + hstepA, voffA);
;         if (wr == 1) PG8_BAR;
;         PG8_WAIT_V(2); PG8_BAR;
;         PG8_STAGE(PG8_SB(1, 0), cB + kstep, voffB); PG8_STAGE(PG8_SA(1, 0), cA + kstep, voffA); PG8_STAGE(PG8_SB(1, 1), cB + hstepB + kstep, voffB);
;         PG8_WAIT_V(6); PG8_BAR;
;     } else {
;         PG8_STAGE(PG8_SB(0, 0), cB, voffB); PG8_STAGE(PG8_SA(0, 0), cA, voffA); PG8_STAGE(PG8_SB(0, 1), cB + hstepB, voffB); PG8_STAGE(PG8_SA(0, 1), cA + hstepA, voffA);
;         if (wr == 1) PG8_BAR;
;         PG8_WAIT_V(4); PG8_BAR;
;         PG8_STAGE(PG8_SB(1, 0), cB + kstep, voffB); PG8_STAGE(PG8_SA(1, 0), cA + kstep, voffA); PG8_STAGE(PG8_SB(1, 1), cB + hstepB + kstep, voffB);
;         PG8_WAIT_V(6); PG8_BAR;
;     }
; __global__ void __launch_bounds__(NTHREADS, 2) fwd(Args args) {
;     ...
;         { pg8::Gemm g{(const bf16_t*)(ws + WS_ACMP), (const bf16_t*)(ws + WS_W_CMP), 2048, 2048, 2048}; pg8::Order<2> S; S.init(16, 2, F.G, F.bid);
;           pg8::EpiF<0> E{nullptr, nullptr, (float*)(ws + WS_HCMP), 512, nullptr, nullptr, 0};
;           pg8::gemm_phase(F.lds, g, S, E); }
.LBB0_317:
	s_cmp_gt_i32 s94, 63
	v_readfirstlane_b32 s9, v0
	s_cbranch_scc1 .LBB0_331
	s_and_b32 s56, s94, 15
	s_mov_b32 s57, 0
	s_lshr_b32 s58, s94, 4
	s_lshl_b32 s59, s58, 10
	s_lshl_b32 s60, s58, 23
	s_lshr_b32 s10, s9, 6
	s_lshr_b32 s14, s9, 8
	s_lshl_b32 s28, s10, 10
	s_add_u32 s29, s88, 0x39400000
	s_addc_u32 s30, s89, 0
	s_add_u32 s31, s88, 0xf000000
	s_addc_u32 s34, s89, 0
	s_waitcnt lgkmcnt(0)
	s_ashr_i32 s0, s56, 3
	s_ashr_i32 s95, s94, 31
	s_ashr_i32 s1, s0, 31
	s_lshl_b64 s[4:5], s[56:57], 20
	s_lshl_b64 s[2:3], s[0:1], 20
	s_add_u32 s2, s31, s2
	s_addc_u32 s3, s34, s3
	s_add_u32 s2, s2, s59
	s_addc_u32 s3, s3, 0
	s_add_u32 s6, s2, 0x80000
	s_addc_u32 s7, s3, 0
	s_add_u32 s4, s29, s4
	s_addc_u32 s5, s30, s5
	s_add_u32 s4, s4, s59
	s_addc_u32 s5, s5, 0
	s_add_u32 s12, s4, 0x80000
	s_addc_u32 s13, s5, 0
	s_add_i32 s1, s28, 0
	v_lshl_or_b32 v132, v230, 12, v229
	s_add_i32 m0, s1, 0x10000
	v_lshl_or_b32 v130, v231, 12, v229
	global_load_lds_dwordx4 v132, s[2:3]
	s_add_i32 m0, s1, 0x12000
	s_add_i32 s35, s1, 0x2000
	global_load_lds_dwordx4 v130, s[2:3]
	s_add_i32 m0, s1, 0x14000
	s_add_i32 s36, s1, 0x4000
	global_load_lds_dwordx4 v132, s[6:7]
	s_add_i32 m0, s1, 0x16000
	s_add_i32 s37, s1, 0x6000
	global_load_lds_dwordx4 v130, s[6:7]
	s_mov_b32 m0, s1
	v_mov_b32_e32 v133, 0
	global_load_lds_dwordx4 v132, s[4:5]
	s_mov_b32 m0, s35
	v_mov_b32_e32 v131, v133
	global_load_lds_dwordx4 v130, s[4:5]
	s_mov_b32 m0, s36
	s_cmp_eq_u32 s14, 1
	global_load_lds_dwordx4 v132, s[12:13]
	s_mov_b32 m0, s37
	v_lshl_add_u64 v[2:3], s[2:3], 0, v[132:133]
	global_load_lds_dwordx4 v130, s[12:13]
	v_lshl_add_u64 v[4:5], s[2:3], 0, v[130:131]
	s_waitcnt vmcnt(0)
	v_lshl_add_u64 v[6:7], s[4:5], 0, v[132:133]
	v_lshl_add_u64 v[8:9], s[4:5], 0, v[130:131]
	s_cselect_b64 s[6:7], -1, 0
	s_cmp_lg_u32 s14, 1
	s_mov_b32 s8, 0
	s_cbranch_scc1 .LBB0_320
	s_barrier
.LBB0_320:
	s_lshl_b32 s10, s10, 5
	s_and_b32 s18, s10, 0x60
	s_lshl_b32 s15, s14, 13
	s_lshl_b32 s19, s18, 7
	s_add_u32 s10, s88, 0x2f400000
	s_addc_u32 s11, s89, 0
	s_add_u32 s10, s10, s60
	s_addc_u32 s11, s11, 0
	s_mov_b64 s[12:13], 0x80
	s_add_u32 s16, s2, 0x80080
	v_lshl_add_u64 v[2:3], v[2:3], 0, s[12:13]
	s_addc_u32 s17, s3, 0
	s_add_i32 m0, s1, 0x18000
	v_lshl_add_u64 v[4:5], v[4:5], 0, s[12:13]
	s_waitcnt vmcnt(2)
	s_barrier
	global_load_lds_dwordx4 v[2:3], off
	s_add_i32 m0, s1, 0x1a000
	s_add_i32 s38, s1, 0x8000
	v_lshl_add_u64 v[6:7], v[6:7], 0, s[12:13]
	global_load_lds_dwordx4 v[4:5], off
	s_mov_b32 m0, s38
	s_add_i32 s39, s1, 0xa000
	v_lshl_add_u64 v[8:9], v[8:9], 0, s[12:13]
	global_load_lds_dwordx4 v[6:7], off
	s_mov_b32 m0, s39
	v_lshl_add_u64 v[10:11], s[16:17], 0, v[132:133]
	global_load_lds_dwordx4 v[8:9], off
	s_add_i32 m0, s1, 0x1c000
	v_lshl_add_u64 v[12:13], s[16:17], 0, v[130:131]
	global_load_lds_dwordx4 v[10:11], off
	s_add_i32 m0, s1, 0x1e000
	v_bfe_u32 v2, v0, 4, 2
	global_load_lds_dwordx4 v[12:13], off
	v_lshlrev_b32_e32 v3, 4, v2
	v_or_b32_e32 v4, v3, v228
	v_lshl_or_b32 v140, v2, 2, s18
	v_lshlrev_b32_e32 v2, 9, v0
	v_bitop3_b32 v139, s19, v4, v227 bitop3:0xf6
	v_and_b32_e32 v2, 0x30000, v2
	v_lshlrev_b32_e32 v4, 12, v224
	v_or3_b32 v2, v1, v2, v4
	v_lshlrev_b32_e32 v5, 2, v226
	v_add_u32_e32 v134, v2, v195
	v_lshlrev_b32_e32 v2, 5, v225
	v_lshl_or_b32 v3, v226, 6, v3
	v_and_b32_e32 v5, 32, v5
	s_waitcnt vmcnt(6)
	s_cmpk_lt_u32 s9, 0x100
	v_and_b32_e32 v2, 0x70000, v2
	v_lshl_or_b32 v138, s14, 6, v226
	v_bitop3_b32 v3, v3, s15, v5 bitop3:0xde
	s_cselect_b64 s[14:15], -1, 0
	v_or3_b32 v1, v1, v2, v4
	s_add_i32 s40, 0, 0x10000
	s_add_i32 s41, 0, 0x14000
	v_mov_b32_e32 v135, v133
	v_add_u32_e32 v136, v1, v195
	v_mov_b32_e32 v137, v133
	s_mov_b64 s[18:19], 0
	v_add_u32_e32 v1, s40, v139
	v_add_u32_e32 v141, s41, v139
	v_add_u32_e32 v142, 0, v3
	s_mov_b64 s[16:17], 0x40000
	s_mov_b32 s42, 0x40000
	s_mov_b32 s44, s56
	s_mov_b32 s43, 0
	s_barrier
	s_branch .LBB0_323

;     __device__ __forceinline__ size_t a_off(const Unit& u, const Gemm& g) const { size_t o = (size_t)u.pm * BM * g.lda * 2; if (MODE == 1) o += (size_t)(u.pn >> 1) * 512 * 2; return o; }
;     __device__ __forceinline__ size_t b_off(const Unit& u, const Gemm& g) const { return (size_t)u.pn * BM * g.ldb * 2; }
; #define PG8_STAGE(bufoff, gbase, voff) do { _Pragma("unroll") for (int _i = 0; _i < 2; ++_i) \
;         __builtin_amdgcn_global_load_lds((const unsigned*)((const char*)(gbase) + (voff)[_i]), (LAS unsigned*)(lds + (bufoff) + ldsw + _i * 8192), 16, 0, 0); } while (0)
; #define PG8_LDA(dst, b, h) do { _Pragma("unroll") for (int m = 0; m < 4; ++m) _Pragma("unroll") for (int k = 0; k < 2; ++k) dst[m][k] = *(const LAS bf16x8*)(lds + PG8_SA(b, h) + aoff + m * 2048 + k * 1024); } while (0)
; #define PG8_WAIT_V(n) asm volatile("s_waitcnt vmcnt(" #n ")" ::: "memory")
; #define PG8_WAIT_L(n) asm volatile("s_waitcnt lgkmcnt(" #n ")" ::: "memory")
;     __device__ bool next(int i, Unit& u) const {
;         const long L = (long)i * G + c; if (L >= nwg) return false;
;         if (MODE == 2) { u.pm = (int)L; u.pn = (int)L >> 3; return true; }
; template <class Epi, class Sched, bool ALIGN_EPI = true, bool SP2 = true, class Side = NoSide>
; __device__ __forceinline__ void gemm_phase(LAS unsigned char* lds, const Gemm g, const Sched& S, const Epi& E, const Side side = Side()) {
;     ...
;     for (;;) {
;         const bool has_next = S.next(ui + 1, nxt);
;         const char* nA = has_next ? (const char*)g.A + S.a_off(nxt, g) : cA; const char* nB = has_next ? (const char*)g.Bt + S.b_off(nxt, g) : cB;
; #pragma unroll 1
;         for (int t = 0; t < nt; t += 2) {
;             const bool last = (t == nt - 2);
;             const char* a1 = cA + (size_t)(t + 1) * kstep;
;             const char* a2 = last ? nA : cA + (size_t)(t + 2) * kstep; const char* b2 = last ? nB : cB + (size_t)(t + 2) * kstep;
;             const char* a3 = a2 + kstep; const char* b3 = b2 + kstep;
;             const bool after_epi = Epi::LOADS && t == 0 && ui > 0;
;             if constexpr (SP2) {
;             PG8_LDB(B0, 0, 0); PG8_LDB(B1, 0, 1); PG8_SCHED; PG8_LDA(At, 0, 0); PG8_STAGE(PG8_SA(1, 1), a1 + hstepA, voffA);
;             if (!after_epi) PG8_WAIT_V(8);
;             PG8_WAIT_L(0); PG8_BAR; PG8_MMA(0, 0, At, B0); PG8_MMA(0, 1, At, B1); PG8_BAR; PG8_SCHED;
.LBB0_323:
	s_mov_b64 s[24:25], s[2:3]
	s_mov_b64 s[2:3], s[18:19]
	s_add_i32 s43, s43, 1
	s_mov_b64 s[22:23], s[4:5]
	s_mov_b32 s3, s0
	s_mov_b32 s45, s0
	s_mul_i32 s0, s43, s33
	s_mul_hi_u32 s4, s43, s96
	s_add_i32 s4, s4, s0
	s_mul_i32 s0, s43, s96
	s_add_u32 s18, s0, s56
	s_addc_u32 s19, s4, s95
	v_cmp_lt_i64_e64 s[20:21], s[18:19], 16
	s_ashr_i32 s0, s18, 3
	s_and_b64 s[4:5], s[20:21], exec
	s_cselect_b32 s9, s18, s2
	s_cselect_b32 s26, s0, s3
	s_ashr_i64 s[2:3], s[8:9], 12
	s_add_u32 s4, s29, s2
	s_addc_u32 s5, s30, s3
	s_and_b64 s[2:3], s[20:21], exec
	s_cselect_b32 s9, s5, s23
	s_cselect_b32 s47, s4, s22
	s_ashr_i32 s27, s26, 31
	s_lshl_b64 s[2:3], s[26:27], 20
	s_add_u32 s2, s31, s2
	s_addc_u32 s3, s34, s3
	s_and_b64 s[26:27], s[20:21], exec
	s_cselect_b32 s48, s3, s25
	s_cselect_b32 s49, s2, s24
	s_add_u32 s22, s22, 0x80080
	s_addc_u32 s23, s23, 0
	s_add_u32 s50, s24, 0x100
	v_mov_b32_e32 v2, 0
	s_mov_b32 s46, s44
	s_mov_b32 s44, s18
	s_addc_u32 s51, s25, 0
	s_mov_b32 s52, -2
	v_mov_b32_e32 v3, v2
	v_mov_b32_e32 v4, v2
	v_mov_b32_e32 v5, v2
	v_mov_b32_e32 v6, v2
	v_mov_b32_e32 v7, v2
	v_mov_b32_e32 v8, v2
	v_mov_b32_e32 v9, v2
	v_mov_b32_e32 v10, v2
	v_mov_b32_e32 v11, v2
	v_mov_b32_e32 v12, v2
	v_mov_b32_e32 v13, v2
	v_mov_b32_e32 v14, v2
	v_mov_b32_e32 v15, v2
	v_mov_b32_e32 v16, v2
	v_mov_b32_e32 v17, v2
	v_mov_b32_e32 v22, v2
	v_mov_b32_e32 v23, v2
	v_mov_b32_e32 v24, v2
	v_mov_b32_e32 v25, v2
	v_mov_b32_e32 v30, v2
	v_mov_b32_e32 v31, v2
	v_mov_b32_e32 v32, v2
	v_mov_b32_e32 v33, v2
	v_mov_b32_e32 v38, v2
	v_mov_b32_e32 v39, v2
	v_mov_b32_e32 v40, v2
	v_mov_b32_e32 v41, v2
	v_mov_b32_e32 v46, v2
	v_mov_b32_e32 v47, v2
	v_mov_b32_e32 v48, v2
	v_mov_b32_e32 v49, v2
	v_mov_b32_e32 v18, v2
	v_mov_b32_e32 v19, v2
	v_mov_b32_e32 v20, v2
	v_mov_b32_e32 v21, v2
	v_mov_b32_e32 v26, v2
	v_mov_b32_e32 v27, v2
	v_mov_b32_e32 v28, v2
	v_mov_b32_e32 v29, v2
	v_mov_b32_e32 v34, v2
	v_mov_b32_e32 v35, v2
	v_mov_b32_e32 v36, v2
	v_mov_b32_e32 v37, v2
	v_mov_b32_e32 v42, v2
	v_mov_b32_e32 v43, v2
	v_mov_b32_e32 v44, v2
	v_mov_b32_e32 v45, v2
	v_mov_b32_e32 v50, v2
	v_mov_b32_e32 v51, v2
	v_mov_b32_e32 v52, v2
	v_mov_b32_e32 v53, v2
	v_mov_b32_e32 v54, v2
	v_mov_b32_e32 v55, v2
	v_mov_b32_e32 v56, v2
	v_mov_b32_e32 v57, v2
	v_mov_b32_e32 v58, v2
	v_mov_b32_e32 v59, v2
	v_mov_b32_e32 v60, v2
	v_mov_b32_e32 v61, v2
	v_mov_b32_e32 v62, v2
	v_mov_b32_e32 v63, v2
	v_mov_b32_e32 v64, v2
	v_mov_b32_e32 v65, v2
	v_mov_b32_e32 v66, v2
	v_mov_b32_e32 v67, v2
	v_mov_b32_e32 v68, v2
	v_mov_b32_e32 v69, v2
	v_mov_b32_e32 v70, v2
	v_mov_b32_e32 v71, v2
	v_mov_b32_e32 v72, v2
	v_mov_b32_e32 v73, v2
	v_mov_b32_e32 v74, v2
	v_mov_b32_e32 v75, v2
	v_mov_b32_e32 v76, v2
	v_mov_b32_e32 v77, v2
	v_mov_b32_e32 v78, v2
	v_mov_b32_e32 v79, v2
	v_mov_b32_e32 v80, v2
	v_mov_b32_e32 v81, v2
	v_mov_b32_e32 v86, v2
	v_mov_b32_e32 v87, v2
	v_mov_b32_e32 v88, v2
	v_mov_b32_e32 v89, v2
	v_mov_b32_e32 v94, v2
	v_mov_b32_e32 v95, v2
	v_mov_b32_e32 v96, v2
	v_mov_b32_e32 v97, v2
	v_mov_b32_e32 v102, v2
	v_mov_b32_e32 v103, v2
	v_mov_b32_e32 v104, v2
	v_mov_b32_e32 v105, v2
	v_mov_b32_e32 v110, v2
	v_mov_b32_e32 v111, v2
	v_mov_b32_e32 v112, v2
	v_mov_b32_e32 v113, v2
	v_mov_b32_e32 v82, v2
	v_mov_b32_e32 v83, v2
	v_mov_b32_e32 v84, v2
	v_mov_b32_e32 v85, v2
	v_mov_b32_e32 v90, v2
	v_mov_b32_e32 v91, v2
	v_mov_b32_e32 v92, v2
	v_mov_b32_e32 v93, v2
	v_mov_b32_e32 v98, v2
	v_mov_b32_e32 v99, v2
	v_mov_b32_e32 v100, v2
	v_mov_b32_e32 v101, v2
	v_mov_b32_e32 v106, v2
	v_mov_b32_e32 v107, v2
	v_mov_b32_e32 v108, v2
	v_mov_b32_e32 v109, v2
	v_mov_b32_e32 v114, v2
	v_mov_b32_e32 v115, v2
	v_mov_b32_e32 v116, v2
	v_mov_b32_e32 v117, v2
	v_mov_b32_e32 v118, v2
	v_mov_b32_e32 v119, v2
	v_mov_b32_e32 v120, v2
	v_mov_b32_e32 v121, v2
	v_mov_b32_e32 v122, v2
	v_mov_b32_e32 v123, v2
	v_mov_b32_e32 v124, v2
	v_mov_b32_e32 v125, v2
	v_mov_b32_e32 v126, v2
	v_mov_b32_e32 v127, v2
	v_mov_b32_e32 v128, v2
	v_mov_b32_e32 v129, v2
.LBB0_324:
	ds_read_b128 v[144:147], v1
	ds_read_b128 v[148:151], v1 offset:1024
	ds_read_b128 v[152:155], v1 offset:2048
	ds_read_b128 v[156:159], v1 offset:3072
	ds_read_b128 v[160:163], v141
	ds_read_b128 v[164:167], v141 offset:1024
	ds_read_b128 v[168:171], v141 offset:2048
	ds_read_b128 v[172:175], v141 offset:3072
	s_add_u32 s24, s22, 0xfff80080
	s_addc_u32 s25, s23, -1
	s_cmp_eq_u32 s52, 4
	s_cselect_b32 s27, s9, s25
	s_cselect_b32 s26, s47, s24
	s_cselect_b32 s25, s48, s51
	s_cselect_b32 s24, s49, s50
	v_lshl_add_u64 v[192:193], s[22:23], 0, v[134:135]
	s_add_i32 m0, s1, 0xc000
	ds_read_b128 v[176:179], v142
	ds_read_b128 v[180:183], v142 offset:1024
	ds_read_b128 v[184:187], v142 offset:2048
	ds_read_b128 v[188:191], v142 offset:3072
	ds_read_b128 v[196:199], v142 offset:4096
	ds_read_b128 v[200:203], v142 offset:5120
	ds_read_b128 v[204:207], v142 offset:6144
	ds_read_b128 v[208:211], v142 offset:7168
	global_load_lds_dwordx4 v[192:193], off
	v_lshl_add_u64 v[192:193], s[22:23], 0, v[136:137]
	s_add_i32 m0, s1, 0xe000
	s_nop 0
	global_load_lds_dwordx4 v[192:193], off
	s_waitcnt vmcnt(8)
	s_waitcnt lgkmcnt(0)
	s_barrier
; #define PG8_STAGE(bufoff, gbase, voff) do { _Pragma("unroll") for (int _i = 0; _i < 2; ++_i) \
;         __builtin_amdgcn_global_load_lds((const unsigned*)((const char*)(gbase) + (voff)[_i]), (LAS unsigned*)(lds + (bufoff) + ldsw + _i * 8192), 16, 0, 0); } while (0)
; #define PG8_LDA(dst, b, h) do { _Pragma("unroll") for (int m = 0; m < 4; ++m) _Pragma("unroll") for (int k = 0; k < 2; ++k) dst[m][k] = *(const LAS bf16x8*)(lds + PG8_SA(b, h) + aoff + m * 2048 + k * 1024); } while (0)
; #define PG8_WAIT_V(n) asm volatile("s_waitcnt vmcnt(" #n ")" ::: "memory")
; #define PG8_WAIT_L(n) asm volatile("s_waitcnt lgkmcnt(" #n ")" ::: "memory")
; #define PG8_BAR __builtin_amdgcn_s_barrier()
; #define PG8_SCHED __builtin_amdgcn_sched_barrier(0)
; template <class Epi, class Sched, bool ALIGN_EPI = true, bool SP2 = true, class Side = NoSide>
; __device__ __forceinline__ void gemm_phase(LAS unsigned char* lds, const Gemm g, const Sched& S, const Epi& E, const Side side = Side()) {
;     ...
;             PG8_WAIT_L(0); PG8_BAR; PG8_MMA(0, 0, At, B0); PG8_MMA(0, 1, At, B1); PG8_BAR; PG8_SCHED;
;             PG8_LDA(At, 0, 1); PG8_STAGE(PG8_SB(0, 0), b2, voffB); PG8_STAGE(PG8_SB(0, 1), b2 + hstepB, voffB); PG8_STAGE(PG8_SA(0, 0), a2, voffA);
;             if (!after_epi) PG8_WAIT_V(8);
;             PG8_WAIT_L(0); PG8_BAR; PG8_MMA(1, 0, At, B0); PG8_MMA(1, 1, At, B1); PG8_BAR; PG8_SCHED;
	s_setprio 1
	s_waitcnt lgkmcnt(0)
	v_mfma_f32_16x16x32_bf16 v[126:129], v[144:147], v[176:179], v[126:129]
	v_mfma_f32_16x16x32_bf16 v[122:125], v[152:155], v[176:179], v[122:125]
	v_mfma_f32_16x16x32_bf16 v[118:121], v[144:147], v[184:187], v[118:121]
	v_mfma_f32_16x16x32_bf16 v[114:117], v[152:155], v[184:187], v[114:117]
	v_mfma_f32_16x16x32_bf16 v[106:109], v[144:147], v[196:199], v[106:109]
	v_mfma_f32_16x16x32_bf16 v[98:101], v[152:155], v[196:199], v[98:101]
	v_mfma_f32_16x16x32_bf16 v[90:93], v[144:147], v[204:207], v[90:93]
	v_mfma_f32_16x16x32_bf16 v[82:85], v[152:155], v[204:207], v[82:85]
	v_mfma_f32_16x16x32_bf16 v[126:129], v[148:151], v[180:183], v[126:129]
	v_mfma_f32_16x16x32_bf16 v[122:125], v[156:159], v[180:183], v[122:125]
	v_mfma_f32_16x16x32_bf16 v[118:121], v[148:151], v[188:191], v[118:121]
	v_mfma_f32_16x16x32_bf16 v[114:117], v[156:159], v[188:191], v[114:117]
	v_mfma_f32_16x16x32_bf16 v[106:109], v[148:151], v[200:203], v[106:109]
	v_mfma_f32_16x16x32_bf16 v[98:101], v[156:159], v[200:203], v[98:101]
	v_mfma_f32_16x16x32_bf16 v[90:93], v[148:151], v[208:211], v[90:93]
	v_mfma_f32_16x16x32_bf16 v[82:85], v[156:159], v[208:211], v[82:85]
	s_setprio 0
	s_setprio 1
	v_mfma_f32_16x16x32_bf16 v[110:113], v[160:163], v[176:179], v[110:113]
	v_mfma_f32_16x16x32_bf16 v[102:105], v[168:171], v[176:179], v[102:105]
	v_mfma_f32_16x16x32_bf16 v[94:97], v[160:163], v[184:187], v[94:97]
	v_mfma_f32_16x16x32_bf16 v[86:89], v[168:171], v[184:187], v[86:89]
	v_mfma_f32_16x16x32_bf16 v[78:81], v[160:163], v[196:199], v[78:81]
	v_mfma_f32_16x16x32_bf16 v[74:77], v[168:171], v[196:199], v[74:77]
	v_mfma_f32_16x16x32_bf16 v[70:73], v[160:163], v[204:207], v[70:73]
	v_mfma_f32_16x16x32_bf16 v[66:69], v[168:171], v[204:207], v[66:69]
	v_mfma_f32_16x16x32_bf16 v[110:113], v[164:167], v[180:183], v[110:113]
	v_mfma_f32_16x16x32_bf16 v[102:105], v[172:175], v[180:183], v[102:105]
	v_mfma_f32_16x16x32_bf16 v[94:97], v[164:167], v[188:191], v[94:97]
	v_mfma_f32_16x16x32_bf16 v[86:89], v[172:175], v[188:191], v[86:89]
	v_mfma_f32_16x16x32_bf16 v[78:81], v[164:167], v[200:203], v[78:81]
	v_mfma_f32_16x16x32_bf16 v[74:77], v[172:175], v[200:203], v[74:77]
	v_mfma_f32_16x16x32_bf16 v[70:73], v[164:167], v[208:211], v[70:73]
	v_mfma_f32_16x16x32_bf16 v[66:69], v[172:175], v[208:211], v[66:69]
	s_setprio 0
	s_barrier
	s_add_i32 s53, s40, s28
	v_lshl_add_u64 v[192:193], s[24:25], 0, v[132:133]
	s_mov_b32 m0, s53
	ds_read_b128 v[176:179], v142 offset:16384
	ds_read_b128 v[180:183], v142 offset:17408
	ds_read_b128 v[184:187], v142 offset:18432
	ds_read_b128 v[188:191], v142 offset:19456
	ds_read_b128 v[196:199], v142 offset:20480
	ds_read_b128 v[200:203], v142 offset:21504
	ds_read_b128 v[204:207], v142 offset:22528
	ds_read_b128 v[208:211], v142 offset:23552
	global_load_lds_dwordx4 v[192:193], off
	s_add_i32 m0, s53, 0x2000
	s_add_u32 s54, s24, 0x80000
	v_lshl_add_u64 v[212:213], s[24:25], 0, v[130:131]
	s_addc_u32 s55, s25, 0
	s_add_i32 s53, s41, s28
	global_load_lds_dwordx4 v[212:213], off
	v_lshl_add_u64 v[214:215], s[54:55], 0, v[132:133]
	s_mov_b32 m0, s53
	v_lshl_add_u64 v[216:217], s[26:27], 0, v[130:131]
	global_load_lds_dwordx4 v[214:215], off
	v_lshl_add_u64 v[214:215], s[54:55], 0, v[130:131]
	s_add_i32 m0, s53, 0x2000
	s_nop 0
	global_load_lds_dwordx4 v[214:215], off
	v_lshl_add_u64 v[214:215], s[26:27], 0, v[132:133]
	s_mov_b32 m0, s1
	s_nop 0
	global_load_lds_dwordx4 v[214:215], off
	s_mov_b32 m0, s35
	s_nop 0
	global_load_lds_dwordx4 v[216:217], off
	s_waitcnt vmcnt(8)
	s_waitcnt lgkmcnt(0)
	s_barrier
	s_setprio 1
	s_waitcnt lgkmcnt(0)
	v_mfma_f32_16x16x32_bf16 v[62:65], v[144:147], v[176:179], v[62:65]
	v_mfma_f32_16x16x32_bf16 v[58:61], v[152:155], v[176:179], v[58:61]
	v_mfma_f32_16x16x32_bf16 v[54:57], v[144:147], v[184:187], v[54:57]
	v_mfma_f32_16x16x32_bf16 v[50:53], v[152:155], v[184:187], v[50:53]
	v_mfma_f32_16x16x32_bf16 v[42:45], v[144:147], v[196:199], v[42:45]
	v_mfma_f32_16x16x32_bf16 v[34:37], v[152:155], v[196:199], v[34:37]
	v_mfma_f32_16x16x32_bf16 v[26:29], v[144:147], v[204:207], v[26:29]
	v_mfma_f32_16x16x32_bf16 v[18:21], v[152:155], v[204:207], v[18:21]
	v_mfma_f32_16x16x32_bf16 v[62:65], v[148:151], v[180:183], v[62:65]
	v_mfma_f32_16x16x32_bf16 v[58:61], v[156:159], v[180:183], v[58:61]
	v_mfma_f32_16x16x32_bf16 v[54:57], v[148:151], v[188:191], v[54:57]
	v_mfma_f32_16x16x32_bf16 v[50:53], v[156:159], v[188:191], v[50:53]
	v_mfma_f32_16x16x32_bf16 v[42:45], v[148:151], v[200:203], v[42:45]
	v_mfma_f32_16x16x32_bf16 v[34:37], v[156:159], v[200:203], v[34:37]
	v_mfma_f32_16x16x32_bf16 v[26:29], v[148:151], v[208:211], v[26:29]
	v_mfma_f32_16x16x32_bf16 v[18:21], v[156:159], v[208:211], v[18:21]
	s_setprio 0
	s_setprio 1
	v_mfma_f32_16x16x32_bf16 v[46:49], v[160:163], v[176:179], v[46:49]
	v_mfma_f32_16x16x32_bf16 v[38:41], v[168:171], v[176:179], v[38:41]
	v_mfma_f32_16x16x32_bf16 v[30:33], v[160:163], v[184:187], v[30:33]
	v_mfma_f32_16x16x32_bf16 v[22:25], v[168:171], v[184:187], v[22:25]
	v_mfma_f32_16x16x32_bf16 v[14:17], v[160:163], v[196:199], v[14:17]
	v_mfma_f32_16x16x32_bf16 v[10:13], v[168:171], v[196:199], v[10:13]
	v_mfma_f32_16x16x32_bf16 v[6:9], v[160:163], v[204:207], v[6:9]
	v_mfma_f32_16x16x32_bf16 v[2:5], v[168:171], v[204:207], v[2:5]
	v_mfma_f32_16x16x32_bf16 v[46:49], v[164:167], v[180:183], v[46:49]
	v_mfma_f32_16x16x32_bf16 v[38:41], v[172:175], v[180:183], v[38:41]
	v_mfma_f32_16x16x32_bf16 v[30:33], v[164:167], v[188:191], v[30:33]
	v_mfma_f32_16x16x32_bf16 v[22:25], v[172:175], v[188:191], v[22:25]
	v_mfma_f32_16x16x32_bf16 v[14:17], v[164:167], v[200:203], v[14:17]
	v_mfma_f32_16x16x32_bf16 v[10:13], v[172:175], v[200:203], v[10:13]
	v_mfma_f32_16x16x32_bf16 v[6:9], v[164:167], v[208:211], v[6:9]
	v_mfma_f32_16x16x32_bf16 v[2:5], v[172:175], v[208:211], v[2:5]
	s_setprio 0
	s_barrier
; #define PG8_STAGE(bufoff, gbase, voff) do { _Pragma("unroll") for (int _i = 0; _i < 2; ++_i) \
;         __builtin_amdgcn_global_load_lds((const unsigned*)((const char*)(gbase) + (voff)[_i]), (LAS unsigned*)(lds + (bufoff) + ldsw + _i * 8192), 16, 0, 0); } while (0)
; #define PG8_LDA(dst, b, h) do { _Pragma("unroll") for (int m = 0; m < 4; ++m) _Pragma("unroll") for (int k = 0; k < 2; ++k) dst[m][k] = *(const LAS bf16x8*)(lds + PG8_SA(b, h) + aoff + m * 2048 + k * 1024); } while (0)
; #define PG8_LDB(dst, b, h) do { _Pragma("unroll") for (int n = 0; n < 2; ++n) _Pragma("unroll") for (int k = 0; k < 2; ++k) dst[n][k] = *(const LAS bf16x8*)(lds + PG8_SB(b, h) + boff + n * 2048 + k * 1024); } while (0)
; #define PG8_WAIT_V(n) asm volatile("s_waitcnt vmcnt(" #n ")" ::: "memory")
; #define PG8_WAIT_L(n) asm volatile("s_waitcnt lgkmcnt(" #n ")" ::: "memory")
; #define PG8_BAR __builtin_amdgcn_s_barrier()
; #define PG8_SCHED __builtin_amdgcn_sched_barrier(0)
; template <class Epi, class Sched, bool ALIGN_EPI = true, bool SP2 = true, class Side = NoSide>
; __device__ __forceinline__ void gemm_phase(LAS unsigned char* lds, const Gemm g, const Sched& S, const Epi& E, const Side side = Side()) {
;     ...
;             PG8_LDB(B0, 1, 0); PG8_LDB(B1, 1, 1); PG8_SCHED; PG8_LDA(At, 1, 0); PG8_STAGE(PG8_SA(0, 1), a2 + hstepA, voffA);
;             PG8_WAIT_V(8); PG8_WAIT_L(0); PG8_BAR; PG8_MMA(0, 0, At, B0); PG8_MMA(0, 1, At, B1); PG8_BAR; PG8_SCHED;
	s_add_i32 s53, 0, 0x18000
	v_add_u32_e32 v143, s53, v139
	s_add_i32 s54, 0, 0x1c000
	ds_read_b128 v[144:147], v143
	ds_read_b128 v[148:151], v143 offset:1024
	ds_read_b128 v[152:155], v143 offset:2048
	ds_read_b128 v[156:159], v143 offset:3072
	v_add_u32_e32 v143, s54, v139
	ds_read_b128 v[160:163], v143
	ds_read_b128 v[164:167], v143 offset:1024
	ds_read_b128 v[168:171], v143 offset:2048
	ds_read_b128 v[172:175], v143 offset:3072
	s_add_u32 s26, s26, 0x80000
	s_addc_u32 s27, s27, 0
	s_mov_b32 m0, s36
	v_lshl_add_u64 v[218:219], s[26:27], 0, v[132:133]
	ds_read_b128 v[176:179], v142 offset:32768
	ds_read_b128 v[180:183], v142 offset:33792
	ds_read_b128 v[184:187], v142 offset:34816
	ds_read_b128 v[188:191], v142 offset:35840
	ds_read_b128 v[196:199], v142 offset:36864
	ds_read_b128 v[200:203], v142 offset:37888
	ds_read_b128 v[204:207], v142 offset:38912
	ds_read_b128 v[208:211], v142 offset:39936
	global_load_lds_dwordx4 v[218:219], off
	v_lshl_add_u64 v[218:219], s[26:27], 0, v[130:131]
	s_mov_b32 m0, s37
	s_nop 0
	global_load_lds_dwordx4 v[218:219], off
	s_waitcnt vmcnt(8)
	s_waitcnt lgkmcnt(0)
	s_barrier
	s_setprio 1
	s_waitcnt lgkmcnt(0)
	v_mfma_f32_16x16x32_bf16 v[126:129], v[144:147], v[176:179], v[126:129]
	v_mfma_f32_16x16x32_bf16 v[122:125], v[152:155], v[176:179], v[122:125]
	v_mfma_f32_16x16x32_bf16 v[118:121], v[144:147], v[184:187], v[118:121]
	v_mfma_f32_16x16x32_bf16 v[114:117], v[152:155], v[184:187], v[114:117]
	v_mfma_f32_16x16x32_bf16 v[106:109], v[144:147], v[196:199], v[106:109]
	v_mfma_f32_16x16x32_bf16 v[98:101], v[152:155], v[196:199], v[98:101]
	v_mfma_f32_16x16x32_bf16 v[90:93], v[144:147], v[204:207], v[90:93]
	v_mfma_f32_16x16x32_bf16 v[82:85], v[152:155], v[204:207], v[82:85]
	v_mfma_f32_16x16x32_bf16 v[126:129], v[148:151], v[180:183], v[126:129]
	v_mfma_f32_16x16x32_bf16 v[122:125], v[156:159], v[180:183], v[122:125]
	v_mfma_f32_16x16x32_bf16 v[118:121], v[148:151], v[188:191], v[118:121]
	v_mfma_f32_16x16x32_bf16 v[114:117], v[156:159], v[188:191], v[114:117]
	v_mfma_f32_16x16x32_bf16 v[106:109], v[148:151], v[200:203], v[106:109]
	v_mfma_f32_16x16x32_bf16 v[98:101], v[156:159], v[200:203], v[98:101]
	v_mfma_f32_16x16x32_bf16 v[90:93], v[148:151], v[208:211], v[90:93]
	v_mfma_f32_16x16x32_bf16 v[82:85], v[156:159], v[208:211], v[82:85]
	s_setprio 0
	s_setprio 1
	v_mfma_f32_16x16x32_bf16 v[110:113], v[160:163], v[176:179], v[110:113]
	v_mfma_f32_16x16x32_bf16 v[102:105], v[168:171], v[176:179], v[102:105]
	v_mfma_f32_16x16x32_bf16 v[94:97], v[160:163], v[184:187], v[94:97]
	v_mfma_f32_16x16x32_bf16 v[86:89], v[168:171], v[184:187], v[86:89]
	v_mfma_f32_16x16x32_bf16 v[78:81], v[160:163], v[196:199], v[78:81]
	v_mfma_f32_16x16x32_bf16 v[74:77], v[168:171], v[196:199], v[74:77]
	v_mfma_f32_16x16x32_bf16 v[70:73], v[160:163], v[204:207], v[70:73]
	v_mfma_f32_16x16x32_bf16 v[66:69], v[168:171], v[204:207], v[66:69]
	v_mfma_f32_16x16x32_bf16 v[110:113], v[164:167], v[180:183], v[110:113]
	v_mfma_f32_16x16x32_bf16 v[102:105], v[172:175], v[180:183], v[102:105]
	v_mfma_f32_16x16x32_bf16 v[94:97], v[164:167], v[188:191], v[94:97]
	v_mfma_f32_16x16x32_bf16 v[86:89], v[172:175], v[188:191], v[86:89]
	v_mfma_f32_16x16x32_bf16 v[78:81], v[164:167], v[200:203], v[78:81]
	v_mfma_f32_16x16x32_bf16 v[74:77], v[172:175], v[200:203], v[74:77]
	v_mfma_f32_16x16x32_bf16 v[70:73], v[164:167], v[208:211], v[70:73]
	v_mfma_f32_16x16x32_bf16 v[66:69], v[172:175], v[208:211], v[66:69]
	s_setprio 0
	s_barrier
; #define PG8_STAGE(bufoff, gbase, voff) do { _Pragma("unroll") for (int _i = 0; _i < 2; ++_i) \
;         __builtin_amdgcn_global_load_lds((const unsigned*)((const char*)(gbase) + (voff)[_i]), (LAS unsigned*)(lds + (bufoff) + ldsw + _i * 8192), 16, 0, 0); } while (0)
; #define PG8_LDA(dst, b, h) do { _Pragma("unroll") for (int m = 0; m < 4; ++m) _Pragma("unroll") for (int k = 0; k < 2; ++k) dst[m][k] = *(const LAS bf16x8*)(lds + PG8_SA(b, h) + aoff + m * 2048 + k * 1024); } while (0)
; #define PG8_WAIT_V(n) asm volatile("s_waitcnt vmcnt(" #n ")" ::: "memory")
; #define PG8_WAIT_L(n) asm volatile("s_waitcnt lgkmcnt(" #n ")" ::: "memory")
; #define PG8_BAR __builtin_amdgcn_s_barrier()
; #define PG8_SCHED __builtin_amdgcn_sched_barrier(0)
; template <class Epi, class Sched, bool ALIGN_EPI = true, bool SP2 = true, class Side = NoSide>
; __device__ __forceinline__ void gemm_phase(LAS unsigned char* lds, const Gemm g, const Sched& S, const Epi& E, const Side side = Side()) {
;     ...
;         for (int t = 0; t < nt; t += 2) {
;             const bool last = (t == nt - 2);
;             const char* a1 = cA + (size_t)(t + 1) * kstep;
;             const char* a2 = last ? nA : cA + (size_t)(t + 2) * kstep; const char* b2 = last ? nB : cB + (size_t)(t + 2) * kstep;
;     ...
;             PG8_LDA(At, 1, 1); PG8_STAGE(PG8_SB(1, 0), b3, voffB); PG8_STAGE(PG8_SB(1, 1), b3 + hstepB, voffB); PG8_STAGE(PG8_SA(1, 0), a3, voffA);
;             PG8_WAIT_V(8); PG8_WAIT_L(0); PG8_BAR; PG8_MMA(1, 0, At, B0); PG8_MMA(1, 1, At, B1); PG8_BAR; PG8_SCHED;
	s_add_i32 s26, s53, s28
	v_lshl_add_u64 v[192:193], v[192:193], 0, s[12:13]
	s_mov_b32 m0, s26
	ds_read_b128 v[176:179], v142 offset:49152
	ds_read_b128 v[180:183], v142 offset:50176
	ds_read_b128 v[184:187], v142 offset:51200
	ds_read_b128 v[188:191], v142 offset:52224
	ds_read_b128 v[196:199], v142 offset:53248
	ds_read_b128 v[200:203], v142 offset:54272
	ds_read_b128 v[204:207], v142 offset:55296
	ds_read_b128 v[208:211], v142 offset:56320
	global_load_lds_dwordx4 v[192:193], off
	s_add_i32 m0, s26, 0x2000
	s_add_u32 s24, s24, 0x80080
	v_lshl_add_u64 v[192:193], v[212:213], 0, s[12:13]
	s_addc_u32 s25, s25, 0
	s_add_i32 s26, s54, s28
	global_load_lds_dwordx4 v[192:193], off
	v_lshl_add_u64 v[192:193], s[24:25], 0, v[132:133]
	s_mov_b32 m0, s26
	s_nop 0
	global_load_lds_dwordx4 v[192:193], off
	v_lshl_add_u64 v[192:193], s[24:25], 0, v[130:131]
	s_add_i32 m0, s26, 0x2000
	s_nop 0
	global_load_lds_dwordx4 v[192:193], off
	v_lshl_add_u64 v[192:193], v[214:215], 0, s[12:13]
	s_mov_b32 m0, s38
	s_nop 0
	global_load_lds_dwordx4 v[192:193], off
	v_lshl_add_u64 v[192:193], v[216:217], 0, s[12:13]
	s_mov_b32 m0, s39
	s_nop 0
	global_load_lds_dwordx4 v[192:193], off
	s_waitcnt vmcnt(8)
	s_waitcnt lgkmcnt(0)
	s_barrier
	s_setprio 1
	s_waitcnt lgkmcnt(0)
	v_mfma_f32_16x16x32_bf16 v[62:65], v[144:147], v[176:179], v[62:65]
	v_mfma_f32_16x16x32_bf16 v[58:61], v[152:155], v[176:179], v[58:61]
	v_mfma_f32_16x16x32_bf16 v[54:57], v[144:147], v[184:187], v[54:57]
	v_mfma_f32_16x16x32_bf16 v[50:53], v[152:155], v[184:187], v[50:53]
	v_mfma_f32_16x16x32_bf16 v[42:45], v[144:147], v[196:199], v[42:45]
	v_mfma_f32_16x16x32_bf16 v[34:37], v[152:155], v[196:199], v[34:37]
	v_mfma_f32_16x16x32_bf16 v[26:29], v[144:147], v[204:207], v[26:29]
	v_mfma_f32_16x16x32_bf16 v[18:21], v[152:155], v[204:207], v[18:21]
	v_mfma_f32_16x16x32_bf16 v[62:65], v[148:151], v[180:183], v[62:65]
	v_mfma_f32_16x16x32_bf16 v[58:61], v[156:159], v[180:183], v[58:61]
	v_mfma_f32_16x16x32_bf16 v[54:57], v[148:151], v[188:191], v[54:57]
	v_mfma_f32_16x16x32_bf16 v[50:53], v[156:159], v[188:191], v[50:53]
	v_mfma_f32_16x16x32_bf16 v[42:45], v[148:151], v[200:203], v[42:45]
	v_mfma_f32_16x16x32_bf16 v[34:37], v[156:159], v[200:203], v[34:37]
	v_mfma_f32_16x16x32_bf16 v[26:29], v[148:151], v[208:211], v[26:29]
	v_mfma_f32_16x16x32_bf16 v[18:21], v[156:159], v[208:211], v[18:21]
	s_setprio 0
	s_setprio 1
	v_mfma_f32_16x16x32_bf16 v[46:49], v[160:163], v[176:179], v[46:49]
	v_mfma_f32_16x16x32_bf16 v[38:41], v[168:171], v[176:179], v[38:41]
	v_mfma_f32_16x16x32_bf16 v[30:33], v[160:163], v[184:187], v[30:33]
	v_mfma_f32_16x16x32_bf16 v[22:25], v[168:171], v[184:187], v[22:25]
	v_mfma_f32_16x16x32_bf16 v[14:17], v[160:163], v[196:199], v[14:17]
	v_mfma_f32_16x16x32_bf16 v[10:13], v[168:171], v[196:199], v[10:13]
	v_mfma_f32_16x16x32_bf16 v[6:9], v[160:163], v[204:207], v[6:9]
	v_mfma_f32_16x16x32_bf16 v[2:5], v[168:171], v[204:207], v[2:5]
	v_mfma_f32_16x16x32_bf16 v[46:49], v[164:167], v[180:183], v[46:49]
	v_mfma_f32_16x16x32_bf16 v[38:41], v[172:175], v[180:183], v[38:41]
	v_mfma_f32_16x16x32_bf16 v[30:33], v[164:167], v[188:191], v[30:33]
	v_mfma_f32_16x16x32_bf16 v[22:25], v[172:175], v[188:191], v[22:25]
	v_mfma_f32_16x16x32_bf16 v[14:17], v[164:167], v[200:203], v[14:17]
	v_mfma_f32_16x16x32_bf16 v[10:13], v[172:175], v[200:203], v[10:13]
	v_mfma_f32_16x16x32_bf16 v[6:9], v[164:167], v[208:211], v[6:9]
	v_mfma_f32_16x16x32_bf16 v[2:5], v[172:175], v[208:211], v[2:5]
	s_setprio 0
	s_barrier
	s_add_i32 s52, s52, 2
	s_add_u32 s22, s22, 0x100
	s_addc_u32 s23, s23, 0
	s_add_u32 s50, s50, 0x100
	s_addc_u32 s51, s51, 0
	s_cmp_gt_u32 s52, 5
	s_cbranch_scc0 .LBB0_324
	s_and_b64 vcc, exec, s[14:15]
	s_cbranch_vccz .LBB0_327
	s_barrier

; __device__ __forceinline__ void phase_cmp_combine(const Frame& F, const Args& a) {
;     unsigned char* ws = a.ws; const float* H = (const float*)(ws + WS_HCMP); const float* bias = (const float*)(ws + WS_SMALL); bf16_t* kcvc = (bf16_t*)(ws + WS_KCVC);
;     const size_t gtid = (size_t)F.bid * NTHREADS + F.tid, gth = (size_t)F.G * NTHREADS;
;     for (size_t i0 = gtid; i0 < (size_t)2 * 4 * 512 * 128; i0 += 4 * gth) { float v[4];
; __global__ void __launch_bounds__(NTHREADS, 2) fwd(Args args) {
;     ...
;     if (IN(4)) for (int rep = 0; rep < REPS(4); ++rep) {
;         phase_cmp_combine(F, args);
.LBB0_381:
	s_cmp_gt_i32 s90, 4
	s_waitcnt lgkmcnt(0)
	s_cselect_b64 s[0:1], -1, 0
	s_cmp_lt_i32 s91, 5
	s_cselect_b64 s[2:3], -1, 0
	s_or_b64 s[0:1], s[0:1], s[2:3]
	s_and_b64 vcc, exec, s[0:1]
	s_cbranch_vccnz .LBB0_528
	s_ashr_i32 s95, s94, 31
	s_lshl_b64 s[0:1], s[94:95], 9
	s_waitcnt vmcnt(0)
	v_or_b32_e32 v2, s0, v0
	v_mov_b32_e32 v3, s1
	s_mov_b64 s[2:3], 0x80000
	v_cmp_gt_u64_e32 vcc, s[2:3], v[2:3]
	s_and_saveexec_b64 s[4:5], vcc
	s_cbranch_execz .LBB0_405
	s_load_dwordx2 s[12:13], s[86:87], 0xc0
	v_and_b32_e32 v2, 0x7f, v0
	v_mov_b32_e32 v7, 0
	v_lshlrev_b32_e32 v6, 2, v2
	s_mov_b64 s[8:9], 0xf200000
	s_waitcnt lgkmcnt(0)
	s_add_u32 s14, s12, 0x2f400000
	s_mov_b32 s46, 0x800000
	s_mov_b32 s47, 0
	s_addc_u32 s15, s13, 0
	s_ashr_i32 s97, s96, 31
	v_lshl_add_u64 v[4:5], s[12:13], 0, v[6:7]
	s_lshl_b64 s[6:7], s[96:97], 9
	v_lshl_add_u64 v[8:9], v[4:5], 0, s[8:9]
	s_lshl_b64 s[8:9], s[94:95], 10
	s_lshl_b64 s[10:11], s[96:97], 10
	s_add_u32 s16, s8, s10
	s_addc_u32 s18, s9, s11
	v_lshlrev_b32_e32 v3, 1, v0
	v_or_b32_e32 v4, s16, v3
	v_mov_b32_e32 v5, s18
	s_mov_b64 s[20:21], 0x3ac00000
	v_lshl_add_u64 v[10:11], v[4:5], 0, s[20:21]
	s_lshl_b64 s[18:19], s[96:97], 12
	v_or_b32_e32 v4, s8, v3
	v_mov_b32_e32 v5, s9
	v_lshl_add_u64 v[12:13], v[4:5], 0, s[20:21]
	s_add_u32 s20, s10, s0
	s_addc_u32 s21, s11, s1
	s_lshl_b64 s[22:23], s[96:97], 11
	s_lshl_b32 s16, s94, 9
	s_lshl_b32 s33, s96, 11
	s_mul_i32 s9, s96, 0x600
	s_mul_hi_i32 s8, s96, 0x600
	s_add_u32 s24, s9, s0
	v_mov_b32_e32 v1, v7
	s_addc_u32 s25, s8, s1
	s_lshl_b32 s8, s96, 9
	v_lshl_add_u64 v[4:5], s[20:21], 0, v[0:1]
	v_mov_b64_e32 v[18:19], 0x3ac00000
	s_add_i32 s40, s9, s16
	s_add_i32 s42, s16, s8
	s_mov_b32 s17, 0
	v_lshl_add_u64 v[16:17], v[4:5], 1, v[18:19]
	v_lshl_add_u64 v[4:5], s[24:25], 0, v[0:1]
	s_add_u32 s26, s0, s6
	v_lshl_or_b32 v14, s96, 10, v0
	s_mov_b32 s41, s17
	v_lshl_add_u64 v[18:19], v[4:5], 1, v[18:19]
	s_mov_b32 s43, s17
	s_addc_u32 s27, s1, s7
	s_mov_b64 s[28:29], 0
	s_movk_i32 s44, 0x1ff
	s_movk_i32 s45, 0x7fff
	s_mov_b64 s[30:31], 0x7ffff
	v_lshlrev_b32_e32 v6, 2, v2
	s_mov_b64 s[34:35], s[16:17]
	s_branch .LBB0_385

; __device__ __forceinline__ void phase_cmp_combine(const Frame& F, const Args& a) {
;     ...
;     for (size_t i0 = gtid; i0 < (size_t)2 * 4 * 512 * 128; i0 += 4 * gth) { float v[4];
; #pragma unroll
;         for (int j = 0; j < 4; ++j) { const size_t i = i0 + (size_t)j * gth; v[j] = 0.f;
;             if (i < (size_t)2 * 4 * 512 * 128) { const int c = (int)(i & 127), n = (int)((i >> 7) & 511), g = (int)((i >> 16) & 3), kv = (int)(i >> 18);
;                 if (n <= 510) { const size_t r = (size_t)kv * 2048 + g * 512 + n; v[j] = H[r * 512 + kv * 256 + c] + H[(r + 1) * 512 + kv * 256 + 128 + c] + bias[kv * 128 + c]; } } }
.LBB0_385:
	v_add_u32_e32 v3, s34, v0
	v_bfe_u32 v3, v3, 7, 9
	v_mov_b32_e32 v2, s17
	v_cmp_ne_u32_e32 vcc, s44, v3
	s_and_saveexec_b64 s[6:7], vcc
	s_cbranch_execz .LBB0_387
	v_lshl_add_u64 v[4:5], v[0:1], 0, s[0:1]
	v_lshrrev_b64 v[20:21], 18, v[4:5]
	v_lshrrev_b32_e32 v2, 7, v4
	v_lshlrev_b64 v[22:23], 11, v[20:21]
	v_and_b32_e32 v2, 0x600, v2
	v_or3_b32 v22, v22, v2, v3
	v_lshlrev_b64 v[2:3], 11, v[22:23]
	v_lshl_add_u64 v[2:3], s[14:15], 0, v[2:3]
	v_lshlrev_b64 v[4:5], 10, v[20:21]
	v_lshl_add_u64 v[2:3], v[2:3], 0, v[4:5]
	v_lshl_add_u64 v[2:3], v[2:3], 0, v[6:7]
	v_lshlrev_b64 v[4:5], 9, v[20:21]
	v_lshl_add_u64 v[4:5], v[8:9], 0, v[4:5]
	v_lshl_add_u64 v[30:31], v[2:3], 0, s[46:47]
	v_lshl_add_u64 v[32:33], v[30:31], 0, s[46:47]
	v_lshl_add_u64 v[34:35], v[32:33], 0, s[46:47]
	global_load_dword v36, v[30:31], off
	global_load_dword v37, v[30:31], off offset:2560
	global_load_dword v38, v[32:33], off
	global_load_dword v39, v[32:33], off offset:2560
	global_load_dword v40, v[34:35], off
	global_load_dword v41, v[34:35], off offset:2560
	global_load_dword v15, v[2:3], off
	s_nop 0
	global_load_dword v2, v[2:3], off offset:2560
	s_nop 0
	global_load_dword v3, v[4:5], off
	s_waitcnt vmcnt(0)
	v_add_f32_e32 v15, v15, v36
	v_add_f32_e32 v15, v15, v38
	v_add_f32_e32 v15, v15, v40
	v_add_f32_e32 v2, v2, v37
	v_add_f32_e32 v2, v2, v39
	v_add_f32_e32 v2, v2, v41
	v_add_f32_e32 v2, v15, v2
	v_add_f32_e32 v2, v2, v3
.LBB0_387:
	s_or_b64 exec, exec, s[6:7]
	v_lshl_add_u64 v[4:5], v[0:1], 0, s[26:27]
	v_mov_b32_e32 v3, s17
	v_cmp_gt_u64_e32 vcc, s[2:3], v[4:5]
	s_and_saveexec_b64 s[8:9], vcc
	s_cbranch_execz .LBB0_391
	v_add_u32_e32 v15, s42, v0
	v_bfe_u32 v15, v15, 7, 9
	v_cmp_ne_u32_e64 s[6:7], s44, v15
	s_and_saveexec_b64 s[10:11], s[6:7]
	s_cbranch_execz .LBB0_390
	v_lshrrev_b64 v[20:21], 18, v[4:5]
	v_lshrrev_b32_e32 v3, 7, v4
	v_lshlrev_b64 v[22:23], 11, v[20:21]
	v_and_b32_e32 v3, 0x600, v3
	v_or3_b32 v22, v22, v3, v15
	v_lshlrev_b64 v[4:5], 11, v[22:23]
	v_lshl_add_u64 v[4:5], s[14:15], 0, v[4:5]
	v_lshlrev_b64 v[22:23], 10, v[20:21]
	v_lshl_add_u64 v[4:5], v[4:5], 0, v[22:23]
	v_lshl_add_u64 v[4:5], v[4:5], 0, v[6:7]
	v_lshlrev_b64 v[20:21], 9, v[20:21]
	v_lshl_add_u64 v[20:21], v[8:9], 0, v[20:21]
	v_lshl_add_u64 v[30:31], v[4:5], 0, s[46:47]
	v_lshl_add_u64 v[32:33], v[30:31], 0, s[46:47]
	v_lshl_add_u64 v[34:35], v[32:33], 0, s[46:47]
	global_load_dword v36, v[30:31], off
	global_load_dword v37, v[30:31], off offset:2560
	global_load_dword v38, v[32:33], off
	global_load_dword v39, v[32:33], off offset:2560
	global_load_dword v40, v[34:35], off
	global_load_dword v41, v[34:35], off offset:2560
	global_load_dword v3, v[4:5], off
	s_nop 0
	global_load_dword v4, v[4:5], off offset:2560
	s_nop 0
	global_load_dword v5, v[20:21], off
	s_waitcnt vmcnt(0)
	v_add_f32_e32 v3, v3, v36
	v_add_f32_e32 v3, v3, v38
	v_add_f32_e32 v3, v3, v40
	v_add_f32_e32 v4, v4, v37
	v_add_f32_e32 v4, v4, v39
	v_add_f32_e32 v4, v4, v41
	v_add_f32_e32 v3, v3, v4
	v_add_f32_e32 v3, v3, v5

; __device__ __forceinline__ void phase_cmp_combine(const Frame& F, const Args& a) {
;     ...
;     for (size_t i0 = gtid; i0 < (size_t)2 * 4 * 512 * 128; i0 += 4 * gth) { float v[4];
; #pragma unroll
;         for (int j = 0; j < 4; ++j) { const size_t i = i0 + (size_t)j * gth; v[j] = 0.f;
;             if (i < (size_t)2 * 4 * 512 * 128) { const int c = (int)(i & 127), n = (int)((i >> 7) & 511), g = (int)((i >> 16) & 3), kv = (int)(i >> 18);
;                 if (n <= 510) { const size_t r = (size_t)kv * 2048 + g * 512 + n; v[j] = H[r * 512 + kv * 256 + c] + H[(r + 1) * 512 + kv * 256 + 128 + c] + bias[kv * 128 + c]; } } }
.LBB0_391:
	s_or_b64 exec, exec, s[8:9]
	v_lshl_add_u64 v[20:21], v[0:1], 0, s[20:21]
	v_mov_b32_e32 v4, s17
	v_cmp_gt_u64_e64 s[6:7], s[2:3], v[20:21]
	s_and_saveexec_b64 s[10:11], s[6:7]
	s_cbranch_execz .LBB0_395
	v_add_u32_e32 v5, s34, v14
	v_bfe_u32 v5, v5, 7, 9
	v_cmp_ne_u32_e64 s[8:9], s44, v5
	s_and_saveexec_b64 s[36:37], s[8:9]
	s_cbranch_execz .LBB0_394
	v_lshrrev_b64 v[22:23], 18, v[20:21]
	v_lshrrev_b32_e32 v4, 7, v20
	v_lshlrev_b64 v[24:25], 11, v[22:23]
	v_and_b32_e32 v4, 0x600, v4
	v_or3_b32 v24, v24, v4, v5
	v_lshlrev_b64 v[4:5], 11, v[24:25]
	v_lshl_add_u64 v[4:5], s[14:15], 0, v[4:5]
	v_lshlrev_b64 v[20:21], 10, v[22:23]
	v_lshl_add_u64 v[4:5], v[4:5], 0, v[20:21]
	v_lshl_add_u64 v[4:5], v[4:5], 0, v[6:7]
	v_lshlrev_b64 v[20:21], 9, v[22:23]
	v_lshl_add_u64 v[20:21], v[8:9], 0, v[20:21]
	v_lshl_add_u64 v[30:31], v[4:5], 0, s[46:47]
	v_lshl_add_u64 v[32:33], v[30:31], 0, s[46:47]
	v_lshl_add_u64 v[34:35], v[32:33], 0, s[46:47]
	global_load_dword v36, v[30:31], off
	global_load_dword v37, v[30:31], off offset:2560
	global_load_dword v38, v[32:33], off
	global_load_dword v39, v[32:33], off offset:2560
	global_load_dword v40, v[34:35], off
	global_load_dword v41, v[34:35], off offset:2560
	global_load_dword v15, v[4:5], off
	s_nop 0
	global_load_dword v4, v[4:5], off offset:2560
	s_nop 0
	global_load_dword v5, v[20:21], off
	s_waitcnt vmcnt(0)
	v_add_f32_e32 v15, v15, v36
	v_add_f32_e32 v15, v15, v38
	v_add_f32_e32 v15, v15, v40
	v_add_f32_e32 v4, v4, v37
	v_add_f32_e32 v4, v4, v39
	v_add_f32_e32 v4, v4, v41
	v_add_f32_e32 v4, v15, v4
	v_add_f32_e32 v4, v4, v5

; __device__ __forceinline__ void phase_cmp_combine(const Frame& F, const Args& a) {
;     ...
;     for (size_t i0 = gtid; i0 < (size_t)2 * 4 * 512 * 128; i0 += 4 * gth) { float v[4];
; #pragma unroll
;         for (int j = 0; j < 4; ++j) { const size_t i = i0 + (size_t)j * gth; v[j] = 0.f;
;             if (i < (size_t)2 * 4 * 512 * 128) { const int c = (int)(i & 127), n = (int)((i >> 7) & 511), g = (int)((i >> 16) & 3), kv = (int)(i >> 18);
;                 if (n <= 510) { const size_t r = (size_t)kv * 2048 + g * 512 + n; v[j] = H[r * 512 + kv * 256 + c] + H[(r + 1) * 512 + kv * 256 + 128 + c] + bias[kv * 128 + c]; } } }
.LBB0_395:
	s_or_b64 exec, exec, s[10:11]
	v_lshl_add_u64 v[20:21], v[0:1], 0, s[24:25]
	v_mov_b32_e32 v5, s17
	v_cmp_gt_u64_e64 s[8:9], s[2:3], v[20:21]
	s_and_saveexec_b64 s[36:37], s[8:9]
	s_cbranch_execz .LBB0_399
	v_add_u32_e32 v15, s40, v0
	v_bfe_u32 v15, v15, 7, 9
	v_cmp_ne_u32_e64 s[10:11], s44, v15
	s_and_saveexec_b64 s[38:39], s[10:11]
	s_cbranch_execz .LBB0_398
	v_lshrrev_b64 v[22:23], 18, v[20:21]
	v_lshrrev_b32_e32 v5, 7, v20
	v_lshlrev_b64 v[24:25], 11, v[22:23]
	v_and_b32_e32 v5, 0x600, v5
	v_or3_b32 v24, v24, v5, v15
	v_lshlrev_b64 v[20:21], 11, v[24:25]
	v_lshl_add_u64 v[20:21], s[14:15], 0, v[20:21]
	v_lshlrev_b64 v[24:25], 10, v[22:23]
	v_lshl_add_u64 v[20:21], v[20:21], 0, v[24:25]
	v_lshl_add_u64 v[20:21], v[20:21], 0, v[6:7]
	v_lshlrev_b64 v[22:23], 9, v[22:23]
	v_lshl_add_u64 v[22:23], v[8:9], 0, v[22:23]
	v_lshl_add_u64 v[30:31], v[20:21], 0, s[46:47]
	v_lshl_add_u64 v[32:33], v[30:31], 0, s[46:47]
	v_lshl_add_u64 v[34:35], v[32:33], 0, s[46:47]
	global_load_dword v36, v[30:31], off
	global_load_dword v37, v[30:31], off offset:2560
	global_load_dword v38, v[32:33], off
	global_load_dword v39, v[32:33], off offset:2560
	global_load_dword v40, v[34:35], off
	global_load_dword v41, v[34:35], off offset:2560
	global_load_dword v5, v[20:21], off
	s_nop 0
	global_load_dword v15, v[20:21], off offset:2560
	s_nop 0
	global_load_dword v20, v[22:23], off
	s_waitcnt vmcnt(0)
	v_add_f32_e32 v5, v5, v36
	v_add_f32_e32 v5, v5, v38
	v_add_f32_e32 v5, v5, v40
	v_add_f32_e32 v15, v15, v37
	v_add_f32_e32 v15, v15, v39
	v_add_f32_e32 v15, v15, v41
	v_add_f32_e32 v5, v5, v15
	v_add_f32_e32 v5, v5, v20
